# v25: v23 + NSA ticket hand-off without the redundant trailing workgroup barrier
# speedup vs baseline: 1.0041x; 1.0041x over previous
.LBB0_702:
	s_or_b64 exec, exec, s[2:3]
	v_mov_b32_e32 v2, s23
	s_waitcnt lgkmcnt(0)
	s_barrier
	ds_read_b32 v2, v2
	v_readlane_b32 s2, v254, 61
	s_waitcnt lgkmcnt(0)
	v_cmp_gt_i32_e32 vcc, s2, v2
	v_readfirstlane_b32 s10, v2
	s_cbranch_vccz .LBB0_988
